# v45 + G1 u8 gate epilogue: the two pre-exp multiplies folded into one constant (256 VALU fewer per gate unit pair)
# baseline (speedup 1.0000x reference)
.LBB0_298:
	s_and_b64 vcc, exec, s[4:5]
	s_cbranch_vccz .LBB0_300
	s_waitcnt lgkmcnt(0)
	v_mul_f32_e32 v2, 0xbcb8aa3b, v136
	v_exp_f32_e32 v4, v2
	v_mul_f32_e32 v6, 0xbcb8aa3b, v137
	v_exp_f32_e32 v6, v6
	v_add_f32_e32 v4, 1.0, v4
	v_rcp_f32_e32 v4, v4
	v_mul_f32_e32 v8, 0xbcb8aa3b, v138
	v_exp_f32_e32 v8, v8
	v_mul_f32_e32 v4, 0x43800000, v4
	v_min_f32_e32 v4, 0x437f0000, v4
	v_cvt_u32_f32_e32 v7, v4
	v_add_f32_e32 v4, 1.0, v6
	v_rcp_f32_e32 v4, v4
	v_mul_f32_e32 v1, 0xbcb8aa3b, v140
	v_mul_f32_e32 v5, 0xbcb8aa3b, v141
	v_mul_f32_e32 v4, 0x43800000, v4
	v_min_f32_e32 v4, 0x437f0000, v4
	v_mul_f32_e32 v6, 0xbcb8aa3b, v142
	v_cvt_u32_f32_e32 v9, v4
	v_add_f32_e32 v4, 1.0, v8
	v_mul_f32_e32 v8, 0xbcb8aa3b, v143
	v_exp_f32_e32 v1, v1
	v_exp_f32_e32 v5, v5
	v_exp_f32_e32 v6, v6
	v_exp_f32_e32 v8, v8
	v_rcp_f32_e32 v4, v4
	v_mul_f32_e32 v10, 0xbcb8aa3b, v139
	v_add_f32_e32 v1, 1.0, v1
	v_add_f32_e32 v5, 1.0, v5
	v_rcp_f32_e32 v1, v1
	v_rcp_f32_e32 v5, v5
	v_add_f32_e32 v6, 1.0, v6
	v_exp_f32_e32 v10, v10
	v_add_f32_e32 v8, 1.0, v8
	v_rcp_f32_e32 v6, v6
	v_rcp_f32_e32 v8, v8
	v_mul_f32_e32 v4, 0x43800000, v4
	v_min_f32_e32 v4, 0x437f0000, v4
	v_mul_f32_e32 v1, 0x43800000, v1
	v_mul_f32_e32 v5, 0x43800000, v5
	v_cvt_u32_f32_sdwa v11, v4 dst_sel:WORD_1 dst_unused:UNUSED_PAD src0_sel:DWORD
	v_add_f32_e32 v4, 1.0, v10
	v_min_f32_e32 v1, 0x437f0000, v1
	v_min_f32_e32 v5, 0x437f0000, v5
	v_mul_f32_e32 v6, 0x43800000, v6
	v_rcp_f32_e32 v4, v4
	v_mul_f32_e32 v8, 0x43800000, v8
	v_cvt_u32_f32_e32 v1, v1
	v_cvt_u32_f32_e32 v5, v5
	v_min_f32_e32 v6, 0x437f0000, v6
	v_min_f32_e32 v8, 0x437f0000, v8
	v_cvt_u32_f32_sdwa v6, v6 dst_sel:WORD_1 dst_unused:UNUSED_PAD src0_sel:DWORD
	v_cvt_u32_f32_sdwa v8, v8 dst_sel:BYTE_3 dst_unused:UNUSED_PAD src0_sel:DWORD
	v_mul_f32_e32 v4, 0x43800000, v4
	v_min_f32_e32 v4, 0x437f0000, v4
	v_lshl_or_b32 v1, v5, 8, v1
	v_cvt_u32_f32_sdwa v10, v4 dst_sel:BYTE_3 dst_unused:UNUSED_PAD src0_sel:DWORD
	v_or3_b32 v4, v1, v6, v8
	v_mul_f32_e32 v6, 0xbcb8aa3b, v128
	s_mul_i32 s4, s68, 24
	s_add_i32 s4, s4, s24
	v_exp_f32_e32 v6, v6
	s_ashr_i32 s5, s4, 31
	s_lshl_b64 s[4:5], s[4:5], 16
	v_lshl_or_b32 v1, v9, 8, v7
	v_lshl_add_u64 v[2:3], v[156:157], 0, s[4:5]
	v_or3_b32 v5, v1, v11, v10
	global_store_dwordx2 v[2:3], v[4:5], off
	v_add_f32_e32 v4, 1.0, v6
	v_rcp_f32_e32 v4, v4
	v_mul_f32_e32 v6, 0xbcb8aa3b, v129
	v_exp_f32_e32 v6, v6
	v_mul_f32_e32 v4, 0x43800000, v4
	v_min_f32_e32 v4, 0x437f0000, v4
	v_cvt_u32_f32_e32 v7, v4
	v_add_f32_e32 v4, 1.0, v6
	v_rcp_f32_e32 v4, v4
	v_mul_f32_e32 v8, 0xbcb8aa3b, v130
	v_exp_f32_e32 v8, v8
	v_mul_f32_e32 v4, 0x43800000, v4
	v_mul_f32_e32 v1, 0xbcb8aa3b, v132
	v_mul_f32_e32 v5, 0xbcb8aa3b, v133
	v_min_f32_e32 v4, 0x437f0000, v4
	v_mul_f32_e32 v6, 0xbcb8aa3b, v134
	v_cvt_u32_f32_e32 v9, v4
	v_add_f32_e32 v4, 1.0, v8
	v_mul_f32_e32 v8, 0xbcb8aa3b, v135
	v_exp_f32_e32 v1, v1
	v_exp_f32_e32 v5, v5
	v_exp_f32_e32 v6, v6
	v_exp_f32_e32 v8, v8
	v_rcp_f32_e32 v4, v4
	v_mul_f32_e32 v10, 0xbcb8aa3b, v131
	v_add_f32_e32 v1, 1.0, v1
	v_add_f32_e32 v5, 1.0, v5
	v_rcp_f32_e32 v1, v1
	v_rcp_f32_e32 v5, v5
	v_add_f32_e32 v6, 1.0, v6
	v_exp_f32_e32 v10, v10
	v_add_f32_e32 v8, 1.0, v8
	v_rcp_f32_e32 v6, v6
	v_rcp_f32_e32 v8, v8
	v_mul_f32_e32 v4, 0x43800000, v4
	v_min_f32_e32 v4, 0x437f0000, v4
	v_mul_f32_e32 v1, 0x43800000, v1
	v_mul_f32_e32 v5, 0x43800000, v5
	v_cvt_u32_f32_sdwa v11, v4 dst_sel:WORD_1 dst_unused:UNUSED_PAD src0_sel:DWORD
	v_add_f32_e32 v4, 1.0, v10
	v_min_f32_e32 v1, 0x437f0000, v1
	v_min_f32_e32 v5, 0x437f0000, v5
	v_mul_f32_e32 v6, 0x43800000, v6
	v_rcp_f32_e32 v4, v4
	v_mul_f32_e32 v8, 0x43800000, v8
	v_cvt_u32_f32_e32 v1, v1
	v_cvt_u32_f32_e32 v5, v5
	v_min_f32_e32 v6, 0x437f0000, v6
	v_min_f32_e32 v8, 0x437f0000, v8
	v_cvt_u32_f32_sdwa v6, v6 dst_sel:WORD_1 dst_unused:UNUSED_PAD src0_sel:DWORD
	v_cvt_u32_f32_sdwa v8, v8 dst_sel:BYTE_3 dst_unused:UNUSED_PAD src0_sel:DWORD
	v_mul_f32_e32 v4, 0x43800000, v4
	v_min_f32_e32 v4, 0x437f0000, v4
	v_lshl_or_b32 v1, v5, 8, v1
	v_cvt_u32_f32_sdwa v10, v4 dst_sel:BYTE_3 dst_unused:UNUSED_PAD src0_sel:DWORD
	v_or3_b32 v4, v1, v6, v8
	v_mul_f32_e32 v6, 0xbcb8aa3b, v120
	v_exp_f32_e32 v6, v6
	v_lshl_or_b32 v1, v9, 8, v7
	v_or3_b32 v5, v1, v11, v10
	global_store_dwordx2 v[2:3], v[4:5], off offset:512
	v_add_f32_e32 v4, 1.0, v6
	v_rcp_f32_e32 v4, v4
	v_mul_f32_e32 v6, 0xbcb8aa3b, v121
	v_exp_f32_e32 v6, v6
	v_mul_f32_e32 v4, 0x43800000, v4
	v_min_f32_e32 v4, 0x437f0000, v4
	v_cvt_u32_f32_e32 v7, v4
	v_add_f32_e32 v4, 1.0, v6
	v_rcp_f32_e32 v4, v4
	v_mul_f32_e32 v8, 0xbcb8aa3b, v122
	v_exp_f32_e32 v8, v8
	v_mul_f32_e32 v4, 0x43800000, v4
	v_mul_f32_e32 v1, 0xbcb8aa3b, v124
	v_mul_f32_e32 v5, 0xbcb8aa3b, v125
	v_min_f32_e32 v4, 0x437f0000, v4
	v_mul_f32_e32 v6, 0xbcb8aa3b, v126
	v_cvt_u32_f32_e32 v9, v4
	v_add_f32_e32 v4, 1.0, v8
	v_mul_f32_e32 v8, 0xbcb8aa3b, v127
	v_exp_f32_e32 v1, v1
	v_exp_f32_e32 v5, v5
	v_exp_f32_e32 v6, v6
	v_exp_f32_e32 v8, v8
	v_rcp_f32_e32 v4, v4
	v_mul_f32_e32 v10, 0xbcb8aa3b, v123
	v_add_f32_e32 v1, 1.0, v1
	v_add_f32_e32 v5, 1.0, v5
	v_rcp_f32_e32 v1, v1
	v_rcp_f32_e32 v5, v5
	v_add_f32_e32 v6, 1.0, v6
	v_exp_f32_e32 v10, v10
	v_add_f32_e32 v8, 1.0, v8
	v_rcp_f32_e32 v6, v6
	v_rcp_f32_e32 v8, v8
	v_mul_f32_e32 v4, 0x43800000, v4
	v_min_f32_e32 v4, 0x437f0000, v4
	v_mul_f32_e32 v1, 0x43800000, v1
	v_mul_f32_e32 v5, 0x43800000, v5
	v_cvt_u32_f32_sdwa v11, v4 dst_sel:WORD_1 dst_unused:UNUSED_PAD src0_sel:DWORD
	v_add_f32_e32 v4, 1.0, v10
	v_min_f32_e32 v1, 0x437f0000, v1
	v_min_f32_e32 v5, 0x437f0000, v5
	v_mul_f32_e32 v6, 0x43800000, v6
	v_rcp_f32_e32 v4, v4
	v_mul_f32_e32 v8, 0x43800000, v8
	v_cvt_u32_f32_e32 v1, v1
	v_cvt_u32_f32_e32 v5, v5
	v_min_f32_e32 v6, 0x437f0000, v6
	v_min_f32_e32 v8, 0x437f0000, v8
	v_cvt_u32_f32_sdwa v6, v6 dst_sel:WORD_1 dst_unused:UNUSED_PAD src0_sel:DWORD
	v_cvt_u32_f32_sdwa v8, v8 dst_sel:BYTE_3 dst_unused:UNUSED_PAD src0_sel:DWORD
	v_mul_f32_e32 v4, 0x43800000, v4
	v_min_f32_e32 v4, 0x437f0000, v4
	v_lshl_or_b32 v1, v5, 8, v1
	v_cvt_u32_f32_sdwa v10, v4 dst_sel:BYTE_3 dst_unused:UNUSED_PAD src0_sel:DWORD
	v_or3_b32 v4, v1, v6, v8
	v_mul_f32_e32 v6, 0xbcb8aa3b, v112
	v_exp_f32_e32 v6, v6
	v_lshl_or_b32 v1, v9, 8, v7
	v_or3_b32 v5, v1, v11, v10
	global_store_dwordx2 v[2:3], v[4:5], off offset:1024
	v_add_f32_e32 v4, 1.0, v6
	v_rcp_f32_e32 v4, v4
	v_mul_f32_e32 v6, 0xbcb8aa3b, v113
	v_exp_f32_e32 v6, v6
	v_mul_f32_e32 v4, 0x43800000, v4
	v_min_f32_e32 v4, 0x437f0000, v4
	v_cvt_u32_f32_e32 v7, v4
	v_add_f32_e32 v4, 1.0, v6
	v_rcp_f32_e32 v4, v4
	v_mul_f32_e32 v8, 0xbcb8aa3b, v114
	v_exp_f32_e32 v8, v8
	v_mul_f32_e32 v4, 0x43800000, v4
	v_mul_f32_e32 v1, 0xbcb8aa3b, v116
	v_mul_f32_e32 v5, 0xbcb8aa3b, v117
	v_min_f32_e32 v4, 0x437f0000, v4
	v_mul_f32_e32 v6, 0xbcb8aa3b, v118
	v_cvt_u32_f32_e32 v9, v4
	v_add_f32_e32 v4, 1.0, v8
	v_mul_f32_e32 v8, 0xbcb8aa3b, v119
	v_exp_f32_e32 v1, v1
	v_exp_f32_e32 v5, v5
	v_exp_f32_e32 v6, v6
	v_exp_f32_e32 v8, v8
	v_rcp_f32_e32 v4, v4
	v_mul_f32_e32 v10, 0xbcb8aa3b, v115
	v_add_f32_e32 v1, 1.0, v1
	v_add_f32_e32 v5, 1.0, v5
	v_rcp_f32_e32 v1, v1
	v_rcp_f32_e32 v5, v5
	v_add_f32_e32 v6, 1.0, v6
	v_exp_f32_e32 v10, v10
	v_add_f32_e32 v8, 1.0, v8
	v_rcp_f32_e32 v6, v6
	v_rcp_f32_e32 v8, v8
	v_mul_f32_e32 v4, 0x43800000, v4
	v_min_f32_e32 v4, 0x437f0000, v4
	v_mul_f32_e32 v1, 0x43800000, v1
	v_mul_f32_e32 v5, 0x43800000, v5
	v_cvt_u32_f32_sdwa v11, v4 dst_sel:WORD_1 dst_unused:UNUSED_PAD src0_sel:DWORD
	v_add_f32_e32 v4, 1.0, v10
	v_min_f32_e32 v1, 0x437f0000, v1
	v_min_f32_e32 v5, 0x437f0000, v5
	v_mul_f32_e32 v6, 0x43800000, v6
	v_rcp_f32_e32 v4, v4
	v_mul_f32_e32 v8, 0x43800000, v8
	v_cvt_u32_f32_e32 v1, v1
	v_cvt_u32_f32_e32 v5, v5
	v_min_f32_e32 v6, 0x437f0000, v6
	v_min_f32_e32 v8, 0x437f0000, v8
	v_cvt_u32_f32_sdwa v6, v6 dst_sel:WORD_1 dst_unused:UNUSED_PAD src0_sel:DWORD
	v_cvt_u32_f32_sdwa v8, v8 dst_sel:BYTE_3 dst_unused:UNUSED_PAD src0_sel:DWORD
	v_mul_f32_e32 v4, 0x43800000, v4
	v_min_f32_e32 v4, 0x437f0000, v4
	v_lshl_or_b32 v1, v5, 8, v1
	v_cvt_u32_f32_sdwa v10, v4 dst_sel:BYTE_3 dst_unused:UNUSED_PAD src0_sel:DWORD
	v_or3_b32 v4, v1, v6, v8
	v_mul_f32_e32 v6, 0xbcb8aa3b, v104
	v_exp_f32_e32 v6, v6
	v_lshl_or_b32 v1, v9, 8, v7
	v_or3_b32 v5, v1, v11, v10
	global_store_dwordx2 v[2:3], v[4:5], off offset:1536
	v_add_f32_e32 v4, 1.0, v6
	v_rcp_f32_e32 v4, v4
	v_mul_f32_e32 v6, 0xbcb8aa3b, v105
	v_exp_f32_e32 v6, v6
	v_mul_f32_e32 v4, 0x43800000, v4
	v_min_f32_e32 v4, 0x437f0000, v4
	v_cvt_u32_f32_e32 v7, v4
	v_add_f32_e32 v4, 1.0, v6
	v_rcp_f32_e32 v4, v4
	v_mul_f32_e32 v8, 0xbcb8aa3b, v106
	v_exp_f32_e32 v8, v8
	v_mul_f32_e32 v4, 0x43800000, v4
	v_mul_f32_e32 v1, 0xbcb8aa3b, v108
	v_mul_f32_e32 v5, 0xbcb8aa3b, v109
	v_min_f32_e32 v4, 0x437f0000, v4
	v_mul_f32_e32 v6, 0xbcb8aa3b, v110
	v_cvt_u32_f32_e32 v9, v4
	v_add_f32_e32 v4, 1.0, v8
	v_mul_f32_e32 v8, 0xbcb8aa3b, v111
	v_exp_f32_e32 v1, v1
	v_exp_f32_e32 v5, v5
	v_exp_f32_e32 v6, v6
	v_exp_f32_e32 v8, v8
	v_rcp_f32_e32 v4, v4
	v_mul_f32_e32 v10, 0xbcb8aa3b, v107
	v_add_f32_e32 v1, 1.0, v1
	v_add_f32_e32 v5, 1.0, v5
	v_rcp_f32_e32 v1, v1
	v_rcp_f32_e32 v5, v5
	v_add_f32_e32 v6, 1.0, v6
	v_exp_f32_e32 v10, v10
	v_add_f32_e32 v8, 1.0, v8
	v_rcp_f32_e32 v6, v6
	v_rcp_f32_e32 v8, v8
	v_mul_f32_e32 v4, 0x43800000, v4
	v_min_f32_e32 v4, 0x437f0000, v4
	v_mul_f32_e32 v1, 0x43800000, v1
	v_mul_f32_e32 v5, 0x43800000, v5
	v_cvt_u32_f32_sdwa v11, v4 dst_sel:WORD_1 dst_unused:UNUSED_PAD src0_sel:DWORD
	v_add_f32_e32 v4, 1.0, v10
	v_min_f32_e32 v1, 0x437f0000, v1
	v_min_f32_e32 v5, 0x437f0000, v5
	v_mul_f32_e32 v6, 0x43800000, v6
	v_rcp_f32_e32 v4, v4
	v_mul_f32_e32 v8, 0x43800000, v8
	v_cvt_u32_f32_e32 v1, v1
	v_cvt_u32_f32_e32 v5, v5
	v_min_f32_e32 v6, 0x437f0000, v6
	v_min_f32_e32 v8, 0x437f0000, v8
	v_cvt_u32_f32_sdwa v6, v6 dst_sel:WORD_1 dst_unused:UNUSED_PAD src0_sel:DWORD
	v_cvt_u32_f32_sdwa v8, v8 dst_sel:BYTE_3 dst_unused:UNUSED_PAD src0_sel:DWORD
	v_mul_f32_e32 v4, 0x43800000, v4
	v_min_f32_e32 v4, 0x437f0000, v4
	v_lshl_or_b32 v1, v5, 8, v1
	v_cvt_u32_f32_sdwa v10, v4 dst_sel:BYTE_3 dst_unused:UNUSED_PAD src0_sel:DWORD
	v_or3_b32 v4, v1, v6, v8
	v_mul_f32_e32 v6, 0xbcb8aa3b, v96
	v_exp_f32_e32 v6, v6
	v_lshl_or_b32 v1, v9, 8, v7
	v_or3_b32 v5, v1, v11, v10
	global_store_dwordx2 v[2:3], v[4:5], off offset:2048
	v_add_f32_e32 v4, 1.0, v6
	v_rcp_f32_e32 v4, v4
	v_mul_f32_e32 v6, 0xbcb8aa3b, v97
	v_exp_f32_e32 v6, v6
	v_mul_f32_e32 v4, 0x43800000, v4
	v_min_f32_e32 v4, 0x437f0000, v4
	v_cvt_u32_f32_e32 v7, v4
	v_add_f32_e32 v4, 1.0, v6
	v_rcp_f32_e32 v4, v4
	v_mul_f32_e32 v8, 0xbcb8aa3b, v98
	v_exp_f32_e32 v8, v8
	v_mul_f32_e32 v4, 0x43800000, v4
	v_mul_f32_e32 v1, 0xbcb8aa3b, v100
	v_mul_f32_e32 v5, 0xbcb8aa3b, v101
	v_min_f32_e32 v4, 0x437f0000, v4
	v_mul_f32_e32 v6, 0xbcb8aa3b, v102
	v_cvt_u32_f32_e32 v9, v4
	v_add_f32_e32 v4, 1.0, v8
	v_mul_f32_e32 v8, 0xbcb8aa3b, v103
	v_exp_f32_e32 v1, v1
	v_exp_f32_e32 v5, v5
	v_exp_f32_e32 v6, v6
	v_exp_f32_e32 v8, v8
	v_rcp_f32_e32 v4, v4
	v_mul_f32_e32 v10, 0xbcb8aa3b, v99
	v_add_f32_e32 v1, 1.0, v1
	v_add_f32_e32 v5, 1.0, v5
	v_rcp_f32_e32 v1, v1
	v_rcp_f32_e32 v5, v5
	v_add_f32_e32 v6, 1.0, v6
	v_exp_f32_e32 v10, v10
	v_add_f32_e32 v8, 1.0, v8
	v_rcp_f32_e32 v6, v6
	v_rcp_f32_e32 v8, v8
	v_mul_f32_e32 v4, 0x43800000, v4
	v_min_f32_e32 v4, 0x437f0000, v4
	v_mul_f32_e32 v1, 0x43800000, v1
	v_mul_f32_e32 v5, 0x43800000, v5
	v_cvt_u32_f32_sdwa v11, v4 dst_sel:WORD_1 dst_unused:UNUSED_PAD src0_sel:DWORD
	v_add_f32_e32 v4, 1.0, v10
	v_min_f32_e32 v1, 0x437f0000, v1
	v_min_f32_e32 v5, 0x437f0000, v5
	v_mul_f32_e32 v6, 0x43800000, v6
	v_rcp_f32_e32 v4, v4
	v_mul_f32_e32 v8, 0x43800000, v8
	v_cvt_u32_f32_e32 v1, v1
	v_cvt_u32_f32_e32 v5, v5
	v_min_f32_e32 v6, 0x437f0000, v6
	v_min_f32_e32 v8, 0x437f0000, v8
	v_cvt_u32_f32_sdwa v6, v6 dst_sel:WORD_1 dst_unused:UNUSED_PAD src0_sel:DWORD
	v_cvt_u32_f32_sdwa v8, v8 dst_sel:BYTE_3 dst_unused:UNUSED_PAD src0_sel:DWORD
	v_mul_f32_e32 v4, 0x43800000, v4
	v_min_f32_e32 v4, 0x437f0000, v4
	v_lshl_or_b32 v1, v5, 8, v1
	v_cvt_u32_f32_sdwa v10, v4 dst_sel:BYTE_3 dst_unused:UNUSED_PAD src0_sel:DWORD
	v_or3_b32 v4, v1, v6, v8
	v_mul_f32_e32 v6, 0xbcb8aa3b, v88
	v_exp_f32_e32 v6, v6
	v_lshl_or_b32 v1, v9, 8, v7
	v_or3_b32 v5, v1, v11, v10
	global_store_dwordx2 v[2:3], v[4:5], off offset:2560
	v_add_f32_e32 v4, 1.0, v6
	v_rcp_f32_e32 v4, v4
	v_mul_f32_e32 v6, 0xbcb8aa3b, v89
	v_exp_f32_e32 v6, v6
	v_mul_f32_e32 v4, 0x43800000, v4
	v_min_f32_e32 v4, 0x437f0000, v4
	v_cvt_u32_f32_e32 v7, v4
	v_add_f32_e32 v4, 1.0, v6
	v_rcp_f32_e32 v4, v4
	v_mul_f32_e32 v8, 0xbcb8aa3b, v90
	v_exp_f32_e32 v8, v8
	v_mul_f32_e32 v4, 0x43800000, v4
	v_mul_f32_e32 v1, 0xbcb8aa3b, v92
	v_mul_f32_e32 v5, 0xbcb8aa3b, v93
	v_min_f32_e32 v4, 0x437f0000, v4
	v_mul_f32_e32 v6, 0xbcb8aa3b, v94
	v_cvt_u32_f32_e32 v9, v4
	v_add_f32_e32 v4, 1.0, v8
	v_mul_f32_e32 v8, 0xbcb8aa3b, v95
	v_exp_f32_e32 v1, v1
	v_exp_f32_e32 v5, v5
	v_exp_f32_e32 v6, v6
	v_exp_f32_e32 v8, v8
	v_rcp_f32_e32 v4, v4
	v_mul_f32_e32 v10, 0xbcb8aa3b, v91
	v_add_f32_e32 v1, 1.0, v1
	v_add_f32_e32 v5, 1.0, v5
	v_rcp_f32_e32 v1, v1
	v_rcp_f32_e32 v5, v5
	v_add_f32_e32 v6, 1.0, v6
	v_exp_f32_e32 v10, v10
	v_add_f32_e32 v8, 1.0, v8
	v_rcp_f32_e32 v6, v6
	v_rcp_f32_e32 v8, v8
	v_mul_f32_e32 v4, 0x43800000, v4
	v_min_f32_e32 v4, 0x437f0000, v4
	v_mul_f32_e32 v1, 0x43800000, v1
	v_mul_f32_e32 v5, 0x43800000, v5
	v_cvt_u32_f32_sdwa v11, v4 dst_sel:WORD_1 dst_unused:UNUSED_PAD src0_sel:DWORD
	v_add_f32_e32 v4, 1.0, v10
	v_min_f32_e32 v1, 0x437f0000, v1
	v_min_f32_e32 v5, 0x437f0000, v5
	v_mul_f32_e32 v6, 0x43800000, v6
	v_rcp_f32_e32 v4, v4
	v_mul_f32_e32 v8, 0x43800000, v8
	v_cvt_u32_f32_e32 v1, v1
	v_cvt_u32_f32_e32 v5, v5
	v_min_f32_e32 v6, 0x437f0000, v6
	v_min_f32_e32 v8, 0x437f0000, v8
	v_cvt_u32_f32_sdwa v6, v6 dst_sel:WORD_1 dst_unused:UNUSED_PAD src0_sel:DWORD
	v_cvt_u32_f32_sdwa v8, v8 dst_sel:BYTE_3 dst_unused:UNUSED_PAD src0_sel:DWORD
	v_mul_f32_e32 v4, 0x43800000, v4
	v_min_f32_e32 v4, 0x437f0000, v4
	v_lshl_or_b32 v1, v5, 8, v1
	v_cvt_u32_f32_sdwa v10, v4 dst_sel:BYTE_3 dst_unused:UNUSED_PAD src0_sel:DWORD
	v_or3_b32 v4, v1, v6, v8
	v_mul_f32_e32 v6, 0xbcb8aa3b, v80
	v_exp_f32_e32 v6, v6
	v_lshl_or_b32 v1, v9, 8, v7
	v_or3_b32 v5, v1, v11, v10
	global_store_dwordx2 v[2:3], v[4:5], off offset:3072
	v_add_f32_e32 v4, 1.0, v6
	v_rcp_f32_e32 v4, v4
	v_mul_f32_e32 v6, 0xbcb8aa3b, v81
	v_exp_f32_e32 v6, v6
	v_mul_f32_e32 v4, 0x43800000, v4
	v_min_f32_e32 v4, 0x437f0000, v4
	v_cvt_u32_f32_e32 v7, v4
	v_add_f32_e32 v4, 1.0, v6
	v_rcp_f32_e32 v4, v4
	v_mul_f32_e32 v8, 0xbcb8aa3b, v82
	v_exp_f32_e32 v8, v8
	v_mul_f32_e32 v4, 0x43800000, v4
	v_mul_f32_e32 v1, 0xbcb8aa3b, v84
	v_mul_f32_e32 v5, 0xbcb8aa3b, v85
	v_min_f32_e32 v4, 0x437f0000, v4
	v_mul_f32_e32 v6, 0xbcb8aa3b, v86
	v_cvt_u32_f32_e32 v9, v4
	v_add_f32_e32 v4, 1.0, v8
	v_mul_f32_e32 v8, 0xbcb8aa3b, v87
	v_exp_f32_e32 v1, v1
	v_exp_f32_e32 v5, v5
	v_exp_f32_e32 v6, v6
	v_exp_f32_e32 v8, v8
	v_rcp_f32_e32 v4, v4
	v_mul_f32_e32 v10, 0xbcb8aa3b, v83
	v_add_f32_e32 v1, 1.0, v1
	v_add_f32_e32 v5, 1.0, v5
	v_rcp_f32_e32 v1, v1
	v_rcp_f32_e32 v5, v5
	v_add_f32_e32 v6, 1.0, v6
	v_exp_f32_e32 v10, v10
	v_add_f32_e32 v8, 1.0, v8
	v_rcp_f32_e32 v6, v6
	v_rcp_f32_e32 v8, v8
	v_mul_f32_e32 v4, 0x43800000, v4
	v_min_f32_e32 v4, 0x437f0000, v4
	v_mul_f32_e32 v1, 0x43800000, v1
	v_mul_f32_e32 v5, 0x43800000, v5
	v_cvt_u32_f32_sdwa v11, v4 dst_sel:WORD_1 dst_unused:UNUSED_PAD src0_sel:DWORD
	v_add_f32_e32 v4, 1.0, v10
	v_min_f32_e32 v1, 0x437f0000, v1
	v_min_f32_e32 v5, 0x437f0000, v5
	v_mul_f32_e32 v6, 0x43800000, v6
	v_rcp_f32_e32 v4, v4
	v_mul_f32_e32 v8, 0x43800000, v8
	v_cvt_u32_f32_e32 v1, v1
	v_cvt_u32_f32_e32 v5, v5
	v_min_f32_e32 v6, 0x437f0000, v6
	v_min_f32_e32 v8, 0x437f0000, v8
	v_cvt_u32_f32_sdwa v6, v6 dst_sel:WORD_1 dst_unused:UNUSED_PAD src0_sel:DWORD
	v_cvt_u32_f32_sdwa v8, v8 dst_sel:BYTE_3 dst_unused:UNUSED_PAD src0_sel:DWORD
	v_mul_f32_e32 v4, 0x43800000, v4
	v_min_f32_e32 v4, 0x437f0000, v4
	v_lshl_or_b32 v1, v5, 8, v1
	v_cvt_u32_f32_sdwa v10, v4 dst_sel:BYTE_3 dst_unused:UNUSED_PAD src0_sel:DWORD
	v_or3_b32 v4, v1, v6, v8
	v_mul_f32_e32 v6, 0xbcb8aa3b, v72
	v_exp_f32_e32 v6, v6
	v_lshl_or_b32 v1, v9, 8, v7
	v_or3_b32 v5, v1, v11, v10
	global_store_dwordx2 v[2:3], v[4:5], off offset:3584
	v_add_f32_e32 v4, 1.0, v6
	v_rcp_f32_e32 v4, v4
	v_mul_f32_e32 v6, 0xbcb8aa3b, v73
	v_exp_f32_e32 v6, v6
	v_mul_f32_e32 v4, 0x43800000, v4
	v_min_f32_e32 v4, 0x437f0000, v4
	v_cvt_u32_f32_e32 v7, v4
	v_add_f32_e32 v4, 1.0, v6
	v_rcp_f32_e32 v4, v4
	v_mul_f32_e32 v8, 0xbcb8aa3b, v74
	v_exp_f32_e32 v8, v8
	v_mul_f32_e32 v4, 0x43800000, v4
	v_mul_f32_e32 v1, 0xbcb8aa3b, v76
	v_mul_f32_e32 v5, 0xbcb8aa3b, v77
	v_min_f32_e32 v4, 0x437f0000, v4
	v_mul_f32_e32 v6, 0xbcb8aa3b, v78
	v_cvt_u32_f32_e32 v9, v4
	v_add_f32_e32 v4, 1.0, v8
	v_mul_f32_e32 v8, 0xbcb8aa3b, v79
	v_exp_f32_e32 v1, v1
	v_exp_f32_e32 v5, v5
	v_exp_f32_e32 v6, v6
	v_exp_f32_e32 v8, v8
	v_rcp_f32_e32 v4, v4
	v_mul_f32_e32 v10, 0xbcb8aa3b, v75
	v_add_f32_e32 v1, 1.0, v1
	v_add_f32_e32 v5, 1.0, v5
	v_rcp_f32_e32 v1, v1
	v_rcp_f32_e32 v5, v5
	v_add_f32_e32 v6, 1.0, v6
	v_exp_f32_e32 v10, v10
	v_add_f32_e32 v8, 1.0, v8
	v_rcp_f32_e32 v6, v6
	v_rcp_f32_e32 v8, v8
	v_mul_f32_e32 v4, 0x43800000, v4
	v_min_f32_e32 v4, 0x437f0000, v4
	v_mul_f32_e32 v1, 0x43800000, v1
	v_mul_f32_e32 v5, 0x43800000, v5
	v_cvt_u32_f32_sdwa v11, v4 dst_sel:WORD_1 dst_unused:UNUSED_PAD src0_sel:DWORD
	v_add_f32_e32 v4, 1.0, v10
	v_min_f32_e32 v1, 0x437f0000, v1
	v_min_f32_e32 v5, 0x437f0000, v5
	v_mul_f32_e32 v6, 0x43800000, v6
	v_rcp_f32_e32 v4, v4
	v_mul_f32_e32 v8, 0x43800000, v8
	v_cvt_u32_f32_e32 v1, v1
	v_cvt_u32_f32_e32 v5, v5
	v_min_f32_e32 v6, 0x437f0000, v6
	v_min_f32_e32 v8, 0x437f0000, v8
	v_cvt_u32_f32_sdwa v6, v6 dst_sel:WORD_1 dst_unused:UNUSED_PAD src0_sel:DWORD
	v_cvt_u32_f32_sdwa v8, v8 dst_sel:BYTE_3 dst_unused:UNUSED_PAD src0_sel:DWORD
	v_mul_f32_e32 v4, 0x43800000, v4
	v_min_f32_e32 v4, 0x437f0000, v4
	v_lshl_or_b32 v1, v5, 8, v1
	v_cvt_u32_f32_sdwa v10, v4 dst_sel:BYTE_3 dst_unused:UNUSED_PAD src0_sel:DWORD
	v_or3_b32 v4, v1, v6, v8
	v_mul_f32_e32 v6, 0xbcb8aa3b, v64
	v_exp_f32_e32 v6, v6
	v_lshl_or_b32 v1, v9, 8, v7
	v_add_co_u32_e32 v2, vcc, s56, v2
	v_or3_b32 v5, v1, v11, v10
	s_nop 0
	v_addc_co_u32_e32 v3, vcc, 0, v3, vcc
	global_store_dwordx2 v[2:3], v[4:5], off
	v_add_f32_e32 v4, 1.0, v6
	v_rcp_f32_e32 v4, v4
	v_mul_f32_e32 v6, 0xbcb8aa3b, v65
	v_exp_f32_e32 v6, v6
	v_mul_f32_e32 v4, 0x43800000, v4
	v_min_f32_e32 v4, 0x437f0000, v4
	v_cvt_u32_f32_e32 v7, v4
	v_add_f32_e32 v4, 1.0, v6
	v_rcp_f32_e32 v4, v4
	v_mul_f32_e32 v8, 0xbcb8aa3b, v66
	v_exp_f32_e32 v8, v8
	v_mul_f32_e32 v4, 0x43800000, v4
	v_mul_f32_e32 v1, 0xbcb8aa3b, v68
	v_mul_f32_e32 v5, 0xbcb8aa3b, v69
	v_min_f32_e32 v4, 0x437f0000, v4
	v_mul_f32_e32 v6, 0xbcb8aa3b, v70
	v_cvt_u32_f32_e32 v9, v4
	v_add_f32_e32 v4, 1.0, v8
	v_mul_f32_e32 v8, 0xbcb8aa3b, v71
	v_exp_f32_e32 v1, v1
	v_exp_f32_e32 v5, v5
	v_exp_f32_e32 v6, v6
	v_exp_f32_e32 v8, v8
	v_rcp_f32_e32 v4, v4
	v_mul_f32_e32 v10, 0xbcb8aa3b, v67
	v_add_f32_e32 v1, 1.0, v1
	v_add_f32_e32 v5, 1.0, v5
	v_rcp_f32_e32 v1, v1
	v_rcp_f32_e32 v5, v5
	v_add_f32_e32 v6, 1.0, v6
	v_exp_f32_e32 v10, v10
	v_add_f32_e32 v8, 1.0, v8
	v_rcp_f32_e32 v6, v6
	v_rcp_f32_e32 v8, v8
	v_mul_f32_e32 v4, 0x43800000, v4
	v_min_f32_e32 v4, 0x437f0000, v4
	v_mul_f32_e32 v1, 0x43800000, v1
	v_mul_f32_e32 v5, 0x43800000, v5
	v_cvt_u32_f32_sdwa v11, v4 dst_sel:WORD_1 dst_unused:UNUSED_PAD src0_sel:DWORD
	v_add_f32_e32 v4, 1.0, v10
	v_min_f32_e32 v1, 0x437f0000, v1
	v_min_f32_e32 v5, 0x437f0000, v5
	v_mul_f32_e32 v6, 0x43800000, v6
	v_rcp_f32_e32 v4, v4
	v_mul_f32_e32 v8, 0x43800000, v8
	v_cvt_u32_f32_e32 v1, v1
	v_cvt_u32_f32_e32 v5, v5
	v_min_f32_e32 v6, 0x437f0000, v6
	v_min_f32_e32 v8, 0x437f0000, v8
	v_cvt_u32_f32_sdwa v6, v6 dst_sel:WORD_1 dst_unused:UNUSED_PAD src0_sel:DWORD
	v_cvt_u32_f32_sdwa v8, v8 dst_sel:BYTE_3 dst_unused:UNUSED_PAD src0_sel:DWORD
	v_mul_f32_e32 v4, 0x43800000, v4
	v_min_f32_e32 v4, 0x437f0000, v4
	v_lshl_or_b32 v1, v5, 8, v1
	v_cvt_u32_f32_sdwa v10, v4 dst_sel:BYTE_3 dst_unused:UNUSED_PAD src0_sel:DWORD
	v_or3_b32 v4, v1, v6, v8
	v_mul_f32_e32 v6, 0xbcb8aa3b, v56
	v_exp_f32_e32 v6, v6
	v_lshl_or_b32 v1, v9, 8, v7
	v_or3_b32 v5, v1, v11, v10
	global_store_dwordx2 v[2:3], v[4:5], off offset:512
	v_add_f32_e32 v4, 1.0, v6
	v_rcp_f32_e32 v4, v4
	v_mul_f32_e32 v6, 0xbcb8aa3b, v57
	v_exp_f32_e32 v6, v6
	v_mul_f32_e32 v4, 0x43800000, v4
	v_min_f32_e32 v4, 0x437f0000, v4
	v_cvt_u32_f32_e32 v7, v4
	v_add_f32_e32 v4, 1.0, v6
	v_rcp_f32_e32 v4, v4
	v_mul_f32_e32 v8, 0xbcb8aa3b, v58
	v_exp_f32_e32 v8, v8
	v_mul_f32_e32 v4, 0x43800000, v4
	v_mul_f32_e32 v1, 0xbcb8aa3b, v60
	v_mul_f32_e32 v5, 0xbcb8aa3b, v61
	v_min_f32_e32 v4, 0x437f0000, v4
	v_mul_f32_e32 v6, 0xbcb8aa3b, v62
	v_cvt_u32_f32_e32 v9, v4
	v_add_f32_e32 v4, 1.0, v8
	v_mul_f32_e32 v8, 0xbcb8aa3b, v63
	v_exp_f32_e32 v1, v1
	v_exp_f32_e32 v5, v5
	v_exp_f32_e32 v6, v6
	v_exp_f32_e32 v8, v8
	v_rcp_f32_e32 v4, v4
	v_mul_f32_e32 v10, 0xbcb8aa3b, v59
	v_add_f32_e32 v1, 1.0, v1
	v_add_f32_e32 v5, 1.0, v5
	v_rcp_f32_e32 v1, v1
	v_rcp_f32_e32 v5, v5
	v_add_f32_e32 v6, 1.0, v6
	v_exp_f32_e32 v10, v10
	v_add_f32_e32 v8, 1.0, v8
	v_rcp_f32_e32 v6, v6
	v_rcp_f32_e32 v8, v8
	v_mul_f32_e32 v4, 0x43800000, v4
	v_min_f32_e32 v4, 0x437f0000, v4
	v_mul_f32_e32 v1, 0x43800000, v1
	v_mul_f32_e32 v5, 0x43800000, v5
	v_cvt_u32_f32_sdwa v11, v4 dst_sel:WORD_1 dst_unused:UNUSED_PAD src0_sel:DWORD
	v_add_f32_e32 v4, 1.0, v10
	v_min_f32_e32 v1, 0x437f0000, v1
	v_min_f32_e32 v5, 0x437f0000, v5
	v_mul_f32_e32 v6, 0x43800000, v6
	v_rcp_f32_e32 v4, v4
	v_mul_f32_e32 v8, 0x43800000, v8
	v_cvt_u32_f32_e32 v1, v1
	v_cvt_u32_f32_e32 v5, v5
	v_min_f32_e32 v6, 0x437f0000, v6
	v_min_f32_e32 v8, 0x437f0000, v8
	v_cvt_u32_f32_sdwa v6, v6 dst_sel:WORD_1 dst_unused:UNUSED_PAD src0_sel:DWORD
	v_cvt_u32_f32_sdwa v8, v8 dst_sel:BYTE_3 dst_unused:UNUSED_PAD src0_sel:DWORD
	v_mul_f32_e32 v4, 0x43800000, v4
	v_min_f32_e32 v4, 0x437f0000, v4
	v_lshl_or_b32 v1, v5, 8, v1
	v_cvt_u32_f32_sdwa v10, v4 dst_sel:BYTE_3 dst_unused:UNUSED_PAD src0_sel:DWORD
	v_or3_b32 v4, v1, v6, v8
	v_mul_f32_e32 v6, 0xbcb8aa3b, v48
	v_exp_f32_e32 v6, v6
	v_lshl_or_b32 v1, v9, 8, v7
	v_or3_b32 v5, v1, v11, v10
	global_store_dwordx2 v[2:3], v[4:5], off offset:1024
	v_add_f32_e32 v4, 1.0, v6
	v_rcp_f32_e32 v4, v4
	v_mul_f32_e32 v6, 0xbcb8aa3b, v49
	v_exp_f32_e32 v6, v6
	v_mul_f32_e32 v4, 0x43800000, v4
	v_min_f32_e32 v4, 0x437f0000, v4
	v_cvt_u32_f32_e32 v7, v4
	v_add_f32_e32 v4, 1.0, v6
	v_rcp_f32_e32 v4, v4
	v_mul_f32_e32 v8, 0xbcb8aa3b, v50
	v_exp_f32_e32 v8, v8
	v_mul_f32_e32 v4, 0x43800000, v4
	v_mul_f32_e32 v1, 0xbcb8aa3b, v52
	v_mul_f32_e32 v5, 0xbcb8aa3b, v53
	v_min_f32_e32 v4, 0x437f0000, v4
	v_mul_f32_e32 v6, 0xbcb8aa3b, v54
	v_cvt_u32_f32_e32 v9, v4
	v_add_f32_e32 v4, 1.0, v8
	v_mul_f32_e32 v8, 0xbcb8aa3b, v55
	v_exp_f32_e32 v1, v1
	v_exp_f32_e32 v5, v5
	v_exp_f32_e32 v6, v6
	v_exp_f32_e32 v8, v8
	v_rcp_f32_e32 v4, v4
	v_mul_f32_e32 v10, 0xbcb8aa3b, v51
	v_add_f32_e32 v1, 1.0, v1
	v_add_f32_e32 v5, 1.0, v5
	v_rcp_f32_e32 v1, v1
	v_rcp_f32_e32 v5, v5
	v_add_f32_e32 v6, 1.0, v6
	v_exp_f32_e32 v10, v10
	v_add_f32_e32 v8, 1.0, v8
	v_rcp_f32_e32 v6, v6
	v_rcp_f32_e32 v8, v8
	v_mul_f32_e32 v4, 0x43800000, v4
	v_min_f32_e32 v4, 0x437f0000, v4
	v_mul_f32_e32 v1, 0x43800000, v1
	v_mul_f32_e32 v5, 0x43800000, v5
	v_cvt_u32_f32_sdwa v11, v4 dst_sel:WORD_1 dst_unused:UNUSED_PAD src0_sel:DWORD
	v_add_f32_e32 v4, 1.0, v10
	v_min_f32_e32 v1, 0x437f0000, v1
	v_min_f32_e32 v5, 0x437f0000, v5
	v_mul_f32_e32 v6, 0x43800000, v6
	v_rcp_f32_e32 v4, v4
	v_mul_f32_e32 v8, 0x43800000, v8
	v_cvt_u32_f32_e32 v1, v1
	v_cvt_u32_f32_e32 v5, v5
	v_min_f32_e32 v6, 0x437f0000, v6
	v_min_f32_e32 v8, 0x437f0000, v8
	v_cvt_u32_f32_sdwa v6, v6 dst_sel:WORD_1 dst_unused:UNUSED_PAD src0_sel:DWORD
	v_cvt_u32_f32_sdwa v8, v8 dst_sel:BYTE_3 dst_unused:UNUSED_PAD src0_sel:DWORD
	v_mul_f32_e32 v4, 0x43800000, v4
	v_min_f32_e32 v4, 0x437f0000, v4
	v_lshl_or_b32 v1, v5, 8, v1
	v_cvt_u32_f32_sdwa v10, v4 dst_sel:BYTE_3 dst_unused:UNUSED_PAD src0_sel:DWORD
	v_or3_b32 v4, v1, v6, v8
	v_mul_f32_e32 v6, 0xbcb8aa3b, v40
	v_exp_f32_e32 v6, v6
	v_lshl_or_b32 v1, v9, 8, v7
	v_or3_b32 v5, v1, v11, v10
	global_store_dwordx2 v[2:3], v[4:5], off offset:1536
	v_add_f32_e32 v4, 1.0, v6
	v_rcp_f32_e32 v4, v4
	v_mul_f32_e32 v6, 0xbcb8aa3b, v41
	v_exp_f32_e32 v6, v6
	v_mul_f32_e32 v4, 0x43800000, v4
	v_min_f32_e32 v4, 0x437f0000, v4
	v_cvt_u32_f32_e32 v7, v4
	v_add_f32_e32 v4, 1.0, v6
	v_rcp_f32_e32 v4, v4
	v_mul_f32_e32 v8, 0xbcb8aa3b, v42
	v_exp_f32_e32 v8, v8
	v_mul_f32_e32 v4, 0x43800000, v4
	v_mul_f32_e32 v1, 0xbcb8aa3b, v44
	v_mul_f32_e32 v5, 0xbcb8aa3b, v45
	v_min_f32_e32 v4, 0x437f0000, v4
	v_mul_f32_e32 v6, 0xbcb8aa3b, v46
	v_cvt_u32_f32_e32 v9, v4
	v_add_f32_e32 v4, 1.0, v8
	v_mul_f32_e32 v8, 0xbcb8aa3b, v47
	v_exp_f32_e32 v1, v1
	v_exp_f32_e32 v5, v5
	v_exp_f32_e32 v6, v6
	v_exp_f32_e32 v8, v8
	v_rcp_f32_e32 v4, v4
	v_mul_f32_e32 v10, 0xbcb8aa3b, v43
	v_add_f32_e32 v1, 1.0, v1
	v_add_f32_e32 v5, 1.0, v5
	v_rcp_f32_e32 v1, v1
	v_rcp_f32_e32 v5, v5
	v_add_f32_e32 v6, 1.0, v6
	v_exp_f32_e32 v10, v10
	v_add_f32_e32 v8, 1.0, v8
	v_rcp_f32_e32 v6, v6
	v_rcp_f32_e32 v8, v8
	v_mul_f32_e32 v4, 0x43800000, v4
	v_min_f32_e32 v4, 0x437f0000, v4
	v_mul_f32_e32 v1, 0x43800000, v1
	v_mul_f32_e32 v5, 0x43800000, v5
	v_cvt_u32_f32_sdwa v11, v4 dst_sel:WORD_1 dst_unused:UNUSED_PAD src0_sel:DWORD
	v_add_f32_e32 v4, 1.0, v10
	v_min_f32_e32 v1, 0x437f0000, v1
	v_min_f32_e32 v5, 0x437f0000, v5
	v_mul_f32_e32 v6, 0x43800000, v6
	v_rcp_f32_e32 v4, v4
	v_mul_f32_e32 v8, 0x43800000, v8
	v_cvt_u32_f32_e32 v1, v1
	v_cvt_u32_f32_e32 v5, v5
	v_min_f32_e32 v6, 0x437f0000, v6
	v_min_f32_e32 v8, 0x437f0000, v8
	v_cvt_u32_f32_sdwa v6, v6 dst_sel:WORD_1 dst_unused:UNUSED_PAD src0_sel:DWORD
	v_cvt_u32_f32_sdwa v8, v8 dst_sel:BYTE_3 dst_unused:UNUSED_PAD src0_sel:DWORD
	v_mul_f32_e32 v4, 0x43800000, v4
	v_min_f32_e32 v4, 0x437f0000, v4
	v_lshl_or_b32 v1, v5, 8, v1
	v_cvt_u32_f32_sdwa v10, v4 dst_sel:BYTE_3 dst_unused:UNUSED_PAD src0_sel:DWORD
	v_or3_b32 v4, v1, v6, v8
	v_mul_f32_e32 v6, 0xbcb8aa3b, v32
	v_exp_f32_e32 v6, v6
	v_lshl_or_b32 v1, v9, 8, v7
	v_or3_b32 v5, v1, v11, v10
	global_store_dwordx2 v[2:3], v[4:5], off offset:2048
	v_add_f32_e32 v4, 1.0, v6
	v_rcp_f32_e32 v4, v4
	v_mul_f32_e32 v6, 0xbcb8aa3b, v33
	v_exp_f32_e32 v6, v6
	v_mul_f32_e32 v4, 0x43800000, v4
	v_min_f32_e32 v4, 0x437f0000, v4
	v_cvt_u32_f32_e32 v7, v4
	v_add_f32_e32 v4, 1.0, v6
	v_rcp_f32_e32 v4, v4
	v_mul_f32_e32 v8, 0xbcb8aa3b, v34
	v_exp_f32_e32 v8, v8
	v_mul_f32_e32 v4, 0x43800000, v4
	v_mul_f32_e32 v1, 0xbcb8aa3b, v36
	v_mul_f32_e32 v5, 0xbcb8aa3b, v37
	v_min_f32_e32 v4, 0x437f0000, v4
	v_mul_f32_e32 v6, 0xbcb8aa3b, v38
	v_cvt_u32_f32_e32 v9, v4
	v_add_f32_e32 v4, 1.0, v8
	v_mul_f32_e32 v8, 0xbcb8aa3b, v39
	v_exp_f32_e32 v1, v1
	v_exp_f32_e32 v5, v5
	v_exp_f32_e32 v6, v6
	v_exp_f32_e32 v8, v8
	v_rcp_f32_e32 v4, v4
	v_mul_f32_e32 v10, 0xbcb8aa3b, v35
	v_add_f32_e32 v1, 1.0, v1
	v_add_f32_e32 v5, 1.0, v5
	v_rcp_f32_e32 v1, v1
	v_rcp_f32_e32 v5, v5
	v_add_f32_e32 v6, 1.0, v6
	v_exp_f32_e32 v10, v10
	v_add_f32_e32 v8, 1.0, v8
	v_rcp_f32_e32 v6, v6
	v_rcp_f32_e32 v8, v8
	v_mul_f32_e32 v4, 0x43800000, v4
	v_min_f32_e32 v4, 0x437f0000, v4
	v_mul_f32_e32 v1, 0x43800000, v1
	v_mul_f32_e32 v5, 0x43800000, v5
	v_cvt_u32_f32_sdwa v11, v4 dst_sel:WORD_1 dst_unused:UNUSED_PAD src0_sel:DWORD
	v_add_f32_e32 v4, 1.0, v10
	v_min_f32_e32 v1, 0x437f0000, v1
	v_min_f32_e32 v5, 0x437f0000, v5
	v_mul_f32_e32 v6, 0x43800000, v6
	v_rcp_f32_e32 v4, v4
	v_mul_f32_e32 v8, 0x43800000, v8
	v_cvt_u32_f32_e32 v1, v1
	v_cvt_u32_f32_e32 v5, v5
	v_min_f32_e32 v6, 0x437f0000, v6
	v_min_f32_e32 v8, 0x437f0000, v8
	v_cvt_u32_f32_sdwa v6, v6 dst_sel:WORD_1 dst_unused:UNUSED_PAD src0_sel:DWORD
	v_cvt_u32_f32_sdwa v8, v8 dst_sel:BYTE_3 dst_unused:UNUSED_PAD src0_sel:DWORD
	v_mul_f32_e32 v4, 0x43800000, v4
	v_min_f32_e32 v4, 0x437f0000, v4
	v_lshl_or_b32 v1, v5, 8, v1
	v_cvt_u32_f32_sdwa v10, v4 dst_sel:BYTE_3 dst_unused:UNUSED_PAD src0_sel:DWORD
	v_or3_b32 v4, v1, v6, v8
	v_mul_f32_e32 v6, 0xbcb8aa3b, v24
	v_exp_f32_e32 v6, v6
	v_lshl_or_b32 v1, v9, 8, v7
	v_or3_b32 v5, v1, v11, v10
	global_store_dwordx2 v[2:3], v[4:5], off offset:2560
	v_add_f32_e32 v4, 1.0, v6
	v_rcp_f32_e32 v4, v4
	v_mul_f32_e32 v6, 0xbcb8aa3b, v25
	v_exp_f32_e32 v6, v6
	v_mul_f32_e32 v4, 0x43800000, v4
	v_min_f32_e32 v4, 0x437f0000, v4
	v_cvt_u32_f32_e32 v7, v4
	v_add_f32_e32 v4, 1.0, v6
	v_rcp_f32_e32 v4, v4
	v_mul_f32_e32 v8, 0xbcb8aa3b, v26
	v_exp_f32_e32 v8, v8
	v_mul_f32_e32 v4, 0x43800000, v4
	v_mul_f32_e32 v1, 0xbcb8aa3b, v28
	v_mul_f32_e32 v5, 0xbcb8aa3b, v29
	v_min_f32_e32 v4, 0x437f0000, v4
	v_mul_f32_e32 v6, 0xbcb8aa3b, v30
	v_cvt_u32_f32_e32 v9, v4
	v_add_f32_e32 v4, 1.0, v8
	v_mul_f32_e32 v8, 0xbcb8aa3b, v31
	v_exp_f32_e32 v1, v1
	v_exp_f32_e32 v5, v5
	v_exp_f32_e32 v6, v6
	v_exp_f32_e32 v8, v8
	v_rcp_f32_e32 v4, v4
	v_mul_f32_e32 v10, 0xbcb8aa3b, v27
	v_add_f32_e32 v1, 1.0, v1
	v_add_f32_e32 v5, 1.0, v5
	v_rcp_f32_e32 v1, v1
	v_rcp_f32_e32 v5, v5
	v_add_f32_e32 v6, 1.0, v6
	v_exp_f32_e32 v10, v10
	v_add_f32_e32 v8, 1.0, v8
	v_rcp_f32_e32 v6, v6
	v_rcp_f32_e32 v8, v8
	v_mul_f32_e32 v4, 0x43800000, v4
	v_min_f32_e32 v4, 0x437f0000, v4
	v_mul_f32_e32 v1, 0x43800000, v1
	v_mul_f32_e32 v5, 0x43800000, v5
	v_cvt_u32_f32_sdwa v11, v4 dst_sel:WORD_1 dst_unused:UNUSED_PAD src0_sel:DWORD
	v_add_f32_e32 v4, 1.0, v10
	v_min_f32_e32 v1, 0x437f0000, v1
	v_min_f32_e32 v5, 0x437f0000, v5
	v_mul_f32_e32 v6, 0x43800000, v6
	v_rcp_f32_e32 v4, v4
	v_mul_f32_e32 v8, 0x43800000, v8
	v_cvt_u32_f32_e32 v1, v1
	v_cvt_u32_f32_e32 v5, v5
	v_min_f32_e32 v6, 0x437f0000, v6
	v_min_f32_e32 v8, 0x437f0000, v8
	v_cvt_u32_f32_sdwa v6, v6 dst_sel:WORD_1 dst_unused:UNUSED_PAD src0_sel:DWORD
	v_cvt_u32_f32_sdwa v8, v8 dst_sel:BYTE_3 dst_unused:UNUSED_PAD src0_sel:DWORD
	v_mul_f32_e32 v4, 0x43800000, v4
	v_min_f32_e32 v4, 0x437f0000, v4
	v_lshl_or_b32 v1, v5, 8, v1
	v_cvt_u32_f32_sdwa v10, v4 dst_sel:BYTE_3 dst_unused:UNUSED_PAD src0_sel:DWORD
	v_or3_b32 v4, v1, v6, v8
	v_mul_f32_e32 v6, 0xbcb8aa3b, v16
	v_exp_f32_e32 v6, v6
	v_lshl_or_b32 v1, v9, 8, v7
	v_or3_b32 v5, v1, v11, v10
	global_store_dwordx2 v[2:3], v[4:5], off offset:3072
	v_add_f32_e32 v4, 1.0, v6
	v_rcp_f32_e32 v4, v4
	v_mul_f32_e32 v6, 0xbcb8aa3b, v17
	v_exp_f32_e32 v6, v6
	v_mul_f32_e32 v4, 0x43800000, v4
	v_min_f32_e32 v4, 0x437f0000, v4
	v_cvt_u32_f32_e32 v7, v4
	v_add_f32_e32 v4, 1.0, v6
	v_rcp_f32_e32 v4, v4
	v_mul_f32_e32 v8, 0xbcb8aa3b, v18
	v_exp_f32_e32 v8, v8
	v_mul_f32_e32 v4, 0x43800000, v4
	v_mul_f32_e32 v1, 0xbcb8aa3b, v20
	v_mul_f32_e32 v5, 0xbcb8aa3b, v21
	v_min_f32_e32 v4, 0x437f0000, v4
	v_mul_f32_e32 v6, 0xbcb8aa3b, v22
	v_cvt_u32_f32_e32 v9, v4
	v_add_f32_e32 v4, 1.0, v8
	v_mul_f32_e32 v8, 0xbcb8aa3b, v23
	v_exp_f32_e32 v1, v1
	v_exp_f32_e32 v5, v5
	v_rcp_f32_e32 v4, v4
	v_mul_f32_e32 v10, 0xbcb8aa3b, v19
	v_exp_f32_e32 v6, v6
	v_exp_f32_e32 v8, v8
	v_exp_f32_e32 v10, v10
	v_add_f32_e32 v1, 1.0, v1
	v_add_f32_e32 v5, 1.0, v5
	v_mul_f32_e32 v4, 0x43800000, v4
	v_rcp_f32_e32 v1, v1
	v_rcp_f32_e32 v5, v5
	v_add_f32_e32 v6, 1.0, v6
	v_min_f32_e32 v4, 0x437f0000, v4
	v_add_f32_e32 v8, 1.0, v8
	v_rcp_f32_e32 v6, v6
	v_rcp_f32_e32 v8, v8
	v_cvt_u32_f32_sdwa v11, v4 dst_sel:WORD_1 dst_unused:UNUSED_PAD src0_sel:DWORD
	v_add_f32_e32 v4, 1.0, v10
	v_rcp_f32_e32 v4, v4
	v_mul_f32_e32 v1, 0x43800000, v1
	v_mul_f32_e32 v5, 0x43800000, v5
	v_min_f32_e32 v1, 0x437f0000, v1
	v_min_f32_e32 v5, 0x437f0000, v5
	v_mul_f32_e32 v6, 0x43800000, v6
	v_mul_f32_e32 v8, 0x43800000, v8
	v_cvt_u32_f32_e32 v1, v1
	v_cvt_u32_f32_e32 v5, v5
	v_min_f32_e32 v6, 0x437f0000, v6
	v_min_f32_e32 v8, 0x437f0000, v8
	v_mul_f32_e32 v4, 0x43800000, v4
	v_cvt_u32_f32_sdwa v6, v6 dst_sel:WORD_1 dst_unused:UNUSED_PAD src0_sel:DWORD
	v_cvt_u32_f32_sdwa v8, v8 dst_sel:BYTE_3 dst_unused:UNUSED_PAD src0_sel:DWORD
	v_min_f32_e32 v4, 0x437f0000, v4
	v_cvt_u32_f32_sdwa v10, v4 dst_sel:BYTE_3 dst_unused:UNUSED_PAD src0_sel:DWORD
	v_lshl_or_b32 v1, v5, 8, v1
	v_or3_b32 v4, v1, v6, v8
	v_lshl_or_b32 v1, v9, 8, v7
	v_or3_b32 v5, v1, v11, v10
	global_store_dwordx2 v[2:3], v[4:5], off offset:3584
